# v56 + thin pass 1: both 4-row trips' loads in flight (second trip pre-issued into renamed registers v144-v195/v228-v241 while the first is computed; counted vmcnt)
# baseline (speedup 1.0000x reference)
; __device__ __forceinline__ void thin_pass(const Ctx& C, const bf16* hin, bf16* hout, bf16* u, float* out, const bf16* y, const float* gpost, float cmul, const float* gpre, bool last) {
;     ...
;     for (int m0 = mstart; m0 < mend; m0 += mstep) {
;         v4u yr[RB][2], hr[RB][2];
; #pragma unroll
;         for (int b = 0; b < RB; ++b) { const v4u* yp = (const v4u*)(y + (size_t)(m0 + b) * D); const v4u* hp = (const v4u*)(hin + (size_t)(m0 + b) * D);
;             yr[b][0] = yp[lane]; yr[b][1] = yp[64 + lane]; hr[b][0] = hp[lane]; hr[b][1] = hp[64 + lane]; }
; #pragma unroll
;         for (int b = 0; b < RB; ++b) {
;             const int m = m0 + b; const v4u y0 = yr[b][0], y1 = yr[b][1], h0 = hr[b][0], h1 = hr[b][1];
;             f32x4 yv[4], h[4];
;             yv[0] = (f32x4){bf_lo(y0.x), bf_hi(y0.x), bf_lo(y0.y), bf_hi(y0.y)}; yv[1] = (f32x4){bf_lo(y0.z), bf_hi(y0.z), bf_lo(y0.w), bf_hi(y0.w)};
;             yv[2] = (f32x4){bf_lo(y1.x), bf_hi(y1.x), bf_lo(y1.y), bf_hi(y1.y)}; yv[3] = (f32x4){bf_lo(y1.z), bf_hi(y1.z), bf_lo(y1.w), bf_hi(y1.w)};
;             h[0] = (f32x4){bf_lo(h0.x), bf_hi(h0.x), bf_lo(h0.y), bf_hi(h0.y)}; h[1] = (f32x4){bf_lo(h0.z), bf_hi(h0.z), bf_lo(h0.w), bf_hi(h0.w)};
;             h[2] = (f32x4){bf_lo(h1.x), bf_hi(h1.x), bf_lo(h1.y), bf_hi(h1.y)}; h[3] = (f32x4){bf_lo(h1.z), bf_hi(h1.z), bf_lo(h1.w), bf_hi(h1.w)};
;             float ss = 0.f;
; #pragma unroll
;             for (int i = 0; i < 4; ++i) ss += (yv[i][0] * yv[i][0] + yv[i][1] * yv[i][1]) + (yv[i][2] * yv[i][2] + yv[i][3] * yv[i][3]);
;             const float ry = cmul / sqrtf(wave_sum(ss) * (1.0f / D) + RMS_EPS);
.LBB0_733:
	s_add_i32 s10, s10, s8
	s_add_u32 s14, s14, s16
	s_addc_u32 s15, s15, s17
	s_add_u32 s18, s18, s16
	s_addc_u32 s19, s19, s17
	s_add_u32 s20, s20, s16
	s_addc_u32 s21, s21, s17
	s_cmp_lt_i32 s10, s0
	v_lshl_add_u64 v[112:113], v[112:113], 0, s[12:13]
	s_cbranch_scc0 .LBB0_750
	s_branch .Lthin1_B
.LBB0_734:
	v_lshl_add_u64 v[114:115], s[14:15], 0, v[100:101]
	v_add_co_u32_e32 v38, vcc, 0xd000000, v114
	v_lshl_add_u64 v[36:37], s[20:21], 0, v[100:101]
	s_nop 0
	v_addc_co_u32_e32 v39, vcc, 0, v115, vcc
	flat_load_dwordx4 v[84:87], v[36:37]
	flat_load_dwordx4 v[88:91], v[36:37] offset:1024
	flat_load_dwordx4 v[92:95], v[38:39] offset:1024
	flat_load_dwordx4 v[96:99], v[38:39]
	s_add_i32 s22, s10, 3
	flat_load_dwordx4 v[80:83], v[36:37] offset:2048
	flat_load_dwordx4 v[68:71], v[36:37] offset:3072
	v_add_co_u32_e32 v36, vcc, s84, v36
	s_ashr_i32 s23, s22, 31
	s_nop 0
	v_addc_co_u32_e32 v37, vcc, 0, v37, vcc
	v_add_co_u32_e32 v56, vcc, s91, v114
	s_lshl_b64 s[2:3], s[22:23], 11
	flat_load_dwordx4 v[64:67], v[36:37]
	flat_load_dwordx4 v[52:55], v[36:37] offset:1024
	v_lshl_add_u64 v[36:37], v[102:103], 0, s[2:3]
	v_lshl_add_u64 v[58:59], v[104:105], 0, s[2:3]
	v_addc_co_u32_e32 v57, vcc, 0, v115, vcc
	flat_load_dwordx4 v[76:79], v[38:39] offset:2048
	flat_load_dwordx4 v[72:75], v[38:39] offset:3072
	flat_load_dwordx4 v[44:47], v[36:37]
	flat_load_dwordx4 v[40:43], v[36:37] offset:1024
	flat_load_dwordx4 v[48:51], v[58:59]
	s_nop 0
	flat_load_dwordx4 v[36:39], v[58:59] offset:1024
	flat_load_dwordx4 v[60:63], v[56:57]
	s_nop 0
	flat_load_dwordx4 v[56:59], v[56:57] offset:1024
	s_add_i32 s42, s10, s8
	s_cmp_lt_i32 s42, s0
	s_cbranch_scc0 .Lthin1_A_nob
	v_lshl_add_u64 v[240:241], s[14:15], 0, v[100:101]
	v_lshl_add_u64 v[240:241], v[240:241], 0, s[16:17]
	v_add_co_u32_e32 v146, vcc, 0xd000000, v240
	v_lshl_add_u64 v[144:145], s[20:21], 0, v[100:101]
	v_lshl_add_u64 v[144:145], v[144:145], 0, s[16:17]
	s_nop 0
	v_addc_co_u32_e32 v147, vcc, 0, v241, vcc
	global_load_dwordx4 v[192:195], v[144:145], off
	global_load_dwordx4 v[228:231], v[144:145], off offset:1024
	global_load_dwordx4 v[232:235], v[146:147], off offset:1024
	global_load_dwordx4 v[236:239], v[146:147], off
	s_add_i32 s42, s10, 3
	s_add_i32 s42, s42, s8
	global_load_dwordx4 v[188:191], v[144:145], off offset:2048
	global_load_dwordx4 v[176:179], v[144:145], off offset:3072
	v_add_co_u32_e32 v144, vcc, s84, v144
	s_ashr_i32 s43, s42, 31
	s_nop 0
	v_addc_co_u32_e32 v145, vcc, 0, v145, vcc
	v_add_co_u32_e32 v164, vcc, s91, v240
	s_lshl_b64 s[2:3], s[42:43], 11
	global_load_dwordx4 v[172:175], v[144:145], off
	global_load_dwordx4 v[160:163], v[144:145], off offset:1024
	v_lshl_add_u64 v[144:145], v[102:103], 0, s[2:3]
	v_lshl_add_u64 v[166:167], v[104:105], 0, s[2:3]
	v_addc_co_u32_e32 v165, vcc, 0, v241, vcc
	global_load_dwordx4 v[184:187], v[146:147], off offset:2048
	global_load_dwordx4 v[180:183], v[146:147], off offset:3072
	global_load_dwordx4 v[152:155], v[144:145], off
	global_load_dwordx4 v[148:151], v[144:145], off offset:1024
	global_load_dwordx4 v[156:159], v[166:167], off
	s_nop 0
	global_load_dwordx4 v[144:147], v[166:167], off offset:1024
	global_load_dwordx4 v[168:171], v[164:165], off
	s_nop 0
	global_load_dwordx4 v[164:167], v[164:165], off offset:1024
	s_waitcnt vmcnt(16) lgkmcnt(0)
	s_branch .Lthin1_A_go
.Lthin1_A_nob:
	s_waitcnt vmcnt(0) lgkmcnt(0)
.Lthin1_A_go:
	v_lshlrev_b32_e32 v118, 16, v86
	v_and_b32_e32 v119, 0xffff0000, v86
	v_lshlrev_b32_e32 v124, 16, v94
	v_and_b32_e32 v142, 0xffff0000, v94
	v_lshlrev_b32_e32 v86, 16, v96
	v_lshlrev_b32_e32 v94, 16, v97
	v_lshlrev_b32_e32 v120, 16, v87
	v_and_b32_e32 v121, 0xffff0000, v87
	v_lshlrev_b32_e32 v122, 16, v88
	v_and_b32_e32 v123, 0xffff0000, v88
	v_lshlrev_b32_e32 v126, 16, v95
	v_and_b32_e32 v127, 0xffff0000, v95
	v_and_b32_e32 v87, 0xffff0000, v96
	v_and_b32_e32 v95, 0xffff0000, v97
	v_lshlrev_b32_e32 v97, 16, v99
	v_lshlrev_b32_e32 v96, 16, v98
	v_and_b32_e32 v99, 0xffff0000, v99
	v_and_b32_e32 v98, 0xffff0000, v98
	v_mul_f32_e32 v2, v86, v86
	v_mul_f32_e32 v88, v94, v94
	v_lshlrev_b32_e32 v128, 16, v92
	v_and_b32_e32 v129, 0xffff0000, v92
	v_lshlrev_b32_e32 v92, 16, v93
	v_pk_mul_f32 v[130:131], v[98:99], v[98:99]
	v_pk_fma_f32 v[138:139], v[86:87], v[86:87], v[2:3] op_sel_hi:[1,1,0]
	v_pk_fma_f32 v[140:141], v[94:95], v[94:95], v[88:89] op_sel_hi:[1,1,0]
	v_and_b32_e32 v93, 0xffff0000, v93
	v_mul_f32_e32 v132, v128, v128
	v_mul_f32_e32 v134, v92, v92
	v_mov_b32_e32 v136, v124
	v_pk_fma_f32 v[130:131], v[96:97], v[96:97], v[130:131]
	v_mov_b32_e32 v125, v139
	v_mov_b32_e32 v137, v141
	v_pk_fma_f32 v[132:133], v[128:129], v[128:129], v[132:133] op_sel_hi:[1,1,0]
	v_pk_fma_f32 v[134:135], v[92:93], v[92:93], v[134:135] op_sel_hi:[1,1,0]
	v_pk_add_f32 v[130:131], v[130:131], v[130:131] op_sel_hi:[0,1]
	v_pk_add_f32 v[138:139], v[138:139], v[140:141]
	v_pk_mul_f32 v[136:137], v[124:125], v[136:137]
	v_mul_f32_e32 v132, v126, v126
	v_mul_f32_e32 v134, v127, v127
	v_mul_f32_e32 v130, v142, v142
	v_mov_b32_e32 v137, v139
	v_pk_add_f32 v[132:133], v[132:133], v[134:135]
	v_pk_add_f32 v[130:131], v[136:137], v[130:131]
	v_lshlrev_b32_e32 v134, 16, v91
	v_pk_add_f32 v[130:131], v[130:131], v[132:133]
	v_lshlrev_b32_e32 v132, 16, v90
	v_add_f32_e32 v2, v130, v131
	v_and_b32_e32 v135, 0xffff0000, v91
	v_lshlrev_b32_e32 v116, 16, v84
	v_add_f32_dpp v2, v2, v2 quad_perm:[1,0,3,2] row_mask:0xf bank_mask:0xf bound_ctrl:1
	v_and_b32_e32 v117, 0xffff0000, v84
	v_lshlrev_b32_e32 v84, 16, v85
; __device__ __forceinline__ unsigned pk2(float lo, float hi) { unsigned r; asm("v_cvt_pk_bf16_f32 %0, %1, %2" : "=v"(r) : "v"(lo), "v"(hi)); return r; }
; __device__ __forceinline__ void thin_pass(const Ctx& C, const bf16* hin, bf16* hout, bf16* u, float* out, const bf16* y, const float* gpost, float cmul, const float* gpre, bool last) {
;     ...
;             const float ry = cmul / sqrtf(wave_sum(ss) * (1.0f / D) + RMS_EPS);
; #pragma unroll
;             for (int i = 0; i < 4; ++i) h[i] = h[i] + yv[i] * ry * g4[i];
;             if (last) { f32x4* op = (f32x4*)(out + (size_t)m * D); op[2 * lane] = h[0]; op[2 * lane + 1] = h[1]; op[128 + 2 * lane] = h[2]; op[128 + 2 * lane + 1] = h[3]; }
;             else {
;                 float s2 = 0.f;
; #pragma unroll
;                 for (int i = 0; i < 4; ++i) s2 += (h[i][0] * h[i][0] + h[i][1] * h[i][1]) + (h[i][2] * h[i][2] + h[i][3] * h[i][3]);
;                 const float rh = 1.0f / sqrtf(wave_sum(s2) * (1.0f / D) + RMS_EPS);
;                 v4u o0, o1; o0.x = pk2(h[0][0], h[0][1]); o0.y = pk2(h[0][2], h[0][3]); o0.z = pk2(h[1][0], h[1][1]); o0.w = pk2(h[1][2], h[1][3]);
;                 o1.x = pk2(h[2][0], h[2][1]); o1.y = pk2(h[2][2], h[2][3]); o1.z = pk2(h[3][0], h[3][1]); o1.w = pk2(h[3][2], h[3][3]);
;                 v4u* hp = (v4u*)(hout + (size_t)m * D); hp[lane] = o0; hp[64 + lane] = o1;
; #pragma unroll
;                 for (int i = 0; i < 4; ++i) h[i] = h[i] * rh * q4[i];
;                 o0.x = pk2(h[0][0], h[0][1]); o0.y = pk2(h[0][2], h[0][3]); o0.z = pk2(h[1][0], h[1][1]); o0.w = pk2(h[1][2], h[1][3]);
;                 o1.x = pk2(h[2][0], h[2][1]); o1.y = pk2(h[2][2], h[2][3]); o1.z = pk2(h[3][0], h[3][1]); o1.w = pk2(h[3][2], h[3][3]);
;                 v4u* up = (v4u*)(u + (size_t)m * D); up[lane] = o0; up[64 + lane] = o1;
	v_add_f32_dpp v2, v2, v2 quad_perm:[2,3,0,1] row_mask:0xf bank_mask:0xf bound_ctrl:1
	v_and_b32_e32 v85, 0xffff0000, v85
	s_nop 0
	v_add_f32_dpp v2, v2, v2 row_half_mirror row_mask:0xf bank_mask:0xf bound_ctrl:1
	s_nop 1
	v_add_f32_dpp v2, v2, v2 row_mirror row_mask:0xf bank_mask:0xf bound_ctrl:1
	s_nop 0
	v_readlane_b32 s1, v2, 16
	v_readlane_b32 s4, v2, 48
	v_readlane_b32 s2, v2, 0
	v_readlane_b32 s3, v2, 32
	v_mov_b32_e32 v130, s1
	v_mov_b32_e32 v131, s4
	v_pk_add_f32 v[130:131], s[2:3], v[130:131]
	s_mov_b64 s[4:5], -1
	v_add_f32_e32 v2, v130, v131
	v_fmamk_f32 v2, v2, 0x3a800000, v214
	v_lshlrev_b32_e32 v130, 16, v89
	v_and_b32_e32 v131, 0xffff0000, v89
	v_and_b32_e32 v133, 0xffff0000, v90
	v_rsq_f32_e32 v2, v2
	s_nop 0
	v_mul_f32_e32 v2, 0.5, v2
	v_pk_mul_f32 v[88:89], v[2:3], v[86:87] op_sel_hi:[0,1]
	v_pk_mul_f32 v[86:87], v[2:3], v[94:95] op_sel_hi:[0,1]
	v_pk_fma_f32 v[86:87], v[10:11], v[86:87], v[84:85]
	v_pk_fma_f32 v[84:85], v[8:9], v[88:89], v[116:117]
	v_mov_b32_e32 v88, v96
	v_mov_b32_e32 v89, v98
	v_mov_b32_e32 v98, v97
	v_pk_mul_f32 v[96:97], v[2:3], v[128:129] op_sel_hi:[0,1]
	v_pk_mul_f32 v[92:93], v[2:3], v[92:93] op_sel_hi:[0,1]
	v_mov_b32_e32 v125, v142
	v_pk_mul_f32 v[88:89], v[2:3], v[88:89] op_sel_hi:[0,1]
	v_pk_mul_f32 v[90:91], v[2:3], v[98:99] op_sel_hi:[0,1]
	v_pk_fma_f32 v[94:95], v[18:19], v[92:93], v[130:131]
	v_pk_fma_f32 v[92:93], v[16:17], v[96:97], v[122:123]
	v_pk_mul_f32 v[96:97], v[124:125], v[2:3] op_sel_hi:[1,0]
	v_pk_mul_f32 v[98:99], v[126:127], v[2:3] op_sel_hi:[1,0]
	v_cndmask_b32_e64 v2, 0, 1, s[6:7]
	v_pk_fma_f32 v[90:91], v[6:7], v[90:91], v[120:121]
	v_pk_fma_f32 v[88:89], v[4:5], v[88:89], v[118:119]
	v_pk_fma_f32 v[98:99], v[14:15], v[98:99], v[134:135]
	v_pk_fma_f32 v[96:97], v[12:13], v[96:97], v[132:133]
	v_cmp_ne_u32_e64 s[2:3], 1, v2
	s_andn2_b64 vcc, exec, s[6:7]
	v_lshl_add_u64 v[116:117], s[18:19], 0, v[100:101]
	s_cbranch_vccnz .LBB0_736
	v_pk_mul_f32 v[118:119], v[86:87], v[86:87]
	v_pk_mul_f32 v[120:121], v[84:85], v[84:85]
	v_mul_f32_e32 v2, v92, v92
	v_pk_mov_b32 v[122:123], v[120:121], v[118:119] op_sel:[1,0]
	v_mov_b32_e32 v121, v119
	v_pk_add_f32 v[118:119], v[122:123], v[120:121]
	v_pk_mul_f32 v[120:121], v[90:91], v[90:91]
	v_pk_mul_f32 v[122:123], v[88:89], v[88:89]
	v_pk_add_f32 v[118:119], v[118:119], v[118:119] op_sel_hi:[0,1]
	v_pk_mov_b32 v[124:125], v[122:123], v[120:121] op_sel:[1,0]
	v_mov_b32_e32 v123, v121
	v_pk_add_f32 v[120:121], v[124:125], v[122:123]
	v_pk_fma_f32 v[122:123], v[92:93], v[92:93], v[2:3] op_sel_hi:[1,1,0]
	v_mul_f32_e32 v2, v94, v94
	v_pk_add_f32 v[120:121], v[120:121], v[120:121] op_sel_hi:[0,1]
	v_pk_fma_f32 v[124:125], v[94:95], v[94:95], v[2:3] op_sel_hi:[1,1,0]
	v_mul_f32_e32 v122, v96, v96
	v_mul_f32_e32 v124, v97, v97
	v_mul_f32_e32 v118, v98, v98
	v_mul_f32_e32 v120, v99, v99
	v_pk_add_f32 v[122:123], v[122:123], v[124:125]
	v_pk_add_f32 v[118:119], v[118:119], v[120:121]
	v_cvt_pk_bf16_f32 v124, v96, v97
	v_cvt_pk_bf16_f32 v125, v98, v99
	s_nop 0
	v_pk_add_f32 v[118:119], v[122:123], v[118:119]
	v_cvt_pk_bf16_f32 v123, v94, v95
	s_nop 0
	v_add_f32_e32 v2, v118, v119
	s_nop 1
	v_add_f32_dpp v2, v2, v2 quad_perm:[1,0,3,2] row_mask:0xf bank_mask:0xf bound_ctrl:1
	s_nop 1
	v_add_f32_dpp v2, v2, v2 quad_perm:[2,3,0,1] row_mask:0xf bank_mask:0xf bound_ctrl:1
	s_nop 1
	v_add_f32_dpp v2, v2, v2 row_half_mirror row_mask:0xf bank_mask:0xf bound_ctrl:1
	s_nop 1
	v_add_f32_dpp v2, v2, v2 row_mirror row_mask:0xf bank_mask:0xf bound_ctrl:1
	s_nop 0
	v_readlane_b32 s1, v2, 16
	v_readlane_b32 s9, v2, 48
	v_readlane_b32 s4, v2, 0
	v_readlane_b32 s5, v2, 32
	v_mov_b32_e32 v118, s1
	v_mov_b32_e32 v119, s9
	v_pk_add_f32 v[118:119], s[4:5], v[118:119]
	s_brev_b32 s1, 64
	v_add_f32_e32 v2, v118, v119
	v_fmamk_f32 v2, v2, 0x3a800000, v214
	s_mov_b64 s[4:5], 0
	v_add_co_u32_e32 v126, vcc, s1, v116
	v_rsq_f32_e32 v2, v2
	s_nop 0
	v_cvt_pk_bf16_f32 v118, v84, v85
	v_cvt_pk_bf16_f32 v119, v86, v87
	v_cvt_pk_bf16_f32 v120, v88, v89
	v_cvt_pk_bf16_f32 v121, v90, v91
	v_cvt_pk_bf16_f32 v122, v92, v93
	s_nop 0
	v_addc_co_u32_e32 v127, vcc, 0, v117, vcc
	global_store_dwordx4 v[126:127], v[118:121], off sc1
	global_store_dwordx4 v[126:127], v[122:125], off offset:1024 sc1
	v_pk_mul_f32 v[126:127], v[92:93], v[2:3] op_sel_hi:[1,0]
	v_pk_mul_f32 v[118:119], v[84:85], v[2:3] op_sel_hi:[1,0]
	v_pk_mul_f32 v[120:121], v[86:87], v[2:3] op_sel_hi:[1,0]
	v_pk_mul_f32 v[122:123], v[88:89], v[2:3] op_sel_hi:[1,0]
	v_pk_mul_f32 v[120:121], v[26:27], v[120:121]
	v_pk_mul_f32 v[118:119], v[24:25], v[118:119]
	v_pk_mul_f32 v[122:123], v[20:21], v[122:123]
	v_pk_mul_f32 v[126:127], v[32:33], v[126:127]
	v_pk_mul_f32 v[124:125], v[90:91], v[2:3] op_sel_hi:[1,0]
	v_cvt_pk_bf16_f32 v118, v118, v119
	v_cvt_pk_bf16_f32 v119, v120, v121
	v_cvt_pk_bf16_f32 v120, v122, v123
	v_cvt_pk_bf16_f32 v122, v126, v127
	v_add_co_u32_e32 v126, vcc, 0xb000000, v114
	v_pk_mul_f32 v[124:125], v[22:23], v[124:125]
	v_pk_mul_f32 v[128:129], v[94:95], v[2:3] op_sel_hi:[1,0]
	v_pk_mul_f32 v[130:131], v[96:97], v[2:3] op_sel_hi:[1,0]
	v_pk_mul_f32 v[132:133], v[98:99], v[2:3] op_sel_hi:[1,0]
	v_cvt_pk_bf16_f32 v121, v124, v125
	v_addc_co_u32_e32 v127, vcc, 0, v115, vcc
	v_pk_mul_f32 v[128:129], v[34:35], v[128:129]
	v_pk_mul_f32 v[132:133], v[30:31], v[132:133]
	v_pk_mul_f32 v[130:131], v[28:29], v[130:131]
	v_cvt_pk_bf16_f32 v123, v128, v129
	v_cvt_pk_bf16_f32 v125, v132, v133
	s_nop 0
	v_cvt_pk_bf16_f32 v124, v130, v131
	flat_store_dwordx4 v[126:127], v[118:121] sc1
	flat_store_dwordx4 v[126:127], v[122:125] offset:1024 sc1

; __device__ __forceinline__ unsigned pk2(float lo, float hi) { unsigned r; asm("v_cvt_pk_bf16_f32 %0, %1, %2" : "=v"(r) : "v"(lo), "v"(hi)); return r; }
; __device__ __forceinline__ void thin_pass(const Ctx& C, const bf16* hin, bf16* hout, bf16* u, float* out, const bf16* y, const float* gpost, float cmul, const float* gpre, bool last) {
;     ...
;         for (int b = 0; b < RB; ++b) {
;             const int m = m0 + b; const v4u y0 = yr[b][0], y1 = yr[b][1], h0 = hr[b][0], h1 = hr[b][1];
;             f32x4 yv[4], h[4];
;             yv[0] = (f32x4){bf_lo(y0.x), bf_hi(y0.x), bf_lo(y0.y), bf_hi(y0.y)}; yv[1] = (f32x4){bf_lo(y0.z), bf_hi(y0.z), bf_lo(y0.w), bf_hi(y0.w)};
;             yv[2] = (f32x4){bf_lo(y1.x), bf_hi(y1.x), bf_lo(y1.y), bf_hi(y1.y)}; yv[3] = (f32x4){bf_lo(y1.z), bf_hi(y1.z), bf_lo(y1.w), bf_hi(y1.w)};
;             h[0] = (f32x4){bf_lo(h0.x), bf_hi(h0.x), bf_lo(h0.y), bf_hi(h0.y)}; h[1] = (f32x4){bf_lo(h0.z), bf_hi(h0.z), bf_lo(h0.w), bf_hi(h0.w)};
;             h[2] = (f32x4){bf_lo(h1.x), bf_hi(h1.x), bf_lo(h1.y), bf_hi(h1.y)}; h[3] = (f32x4){bf_lo(h1.z), bf_hi(h1.z), bf_lo(h1.w), bf_hi(h1.w)};
;             float ss = 0.f;
; #pragma unroll
;             for (int i = 0; i < 4; ++i) ss += (yv[i][0] * yv[i][0] + yv[i][1] * yv[i][1]) + (yv[i][2] * yv[i][2] + yv[i][3] * yv[i][3]);
;             const float ry = cmul / sqrtf(wave_sum(ss) * (1.0f / D) + RMS_EPS);
; #pragma unroll
;             for (int i = 0; i < 4; ++i) h[i] = h[i] + yv[i] * ry * g4[i];
;             if (last) { f32x4* op = (f32x4*)(out + (size_t)m * D); op[2 * lane] = h[0]; op[2 * lane + 1] = h[1]; op[128 + 2 * lane] = h[2]; op[128 + 2 * lane + 1] = h[3]; }
;             else {
;                 float s2 = 0.f;
; #pragma unroll
;                 for (int i = 0; i < 4; ++i) s2 += (h[i][0] * h[i][0] + h[i][1] * h[i][1]) + (h[i][2] * h[i][2] + h[i][3] * h[i][3]);
;                 const float rh = 1.0f / sqrtf(wave_sum(s2) * (1.0f / D) + RMS_EPS);
;                 v4u o0, o1; o0.x = pk2(h[0][0], h[0][1]); o0.y = pk2(h[0][2], h[0][3]); o0.z = pk2(h[1][0], h[1][1]); o0.w = pk2(h[1][2], h[1][3]);
;                 o1.x = pk2(h[2][0], h[2][1]); o1.y = pk2(h[2][2], h[2][3]); o1.z = pk2(h[3][0], h[3][1]); o1.w = pk2(h[3][2], h[3][3]);
.Lthin1_B:
	s_waitcnt vmcnt(12)
	v_lshlrev_b32_e32 v118, 16, v194
	v_and_b32_e32 v119, 0xffff0000, v194
	v_lshlrev_b32_e32 v124, 16, v234
	v_and_b32_e32 v142, 0xffff0000, v234
	v_lshlrev_b32_e32 v194, 16, v236
	v_lshlrev_b32_e32 v234, 16, v237
	v_lshlrev_b32_e32 v120, 16, v195
	v_and_b32_e32 v121, 0xffff0000, v195
	v_lshlrev_b32_e32 v122, 16, v228
	v_and_b32_e32 v123, 0xffff0000, v228
	v_lshlrev_b32_e32 v126, 16, v235
	v_and_b32_e32 v127, 0xffff0000, v235
	v_and_b32_e32 v195, 0xffff0000, v236
	v_and_b32_e32 v235, 0xffff0000, v237
	v_lshlrev_b32_e32 v237, 16, v239
	v_lshlrev_b32_e32 v236, 16, v238
	v_and_b32_e32 v239, 0xffff0000, v239
	v_and_b32_e32 v238, 0xffff0000, v238
	v_mul_f32_e32 v2, v194, v194
	v_mul_f32_e32 v228, v234, v234
	v_lshlrev_b32_e32 v128, 16, v232
	v_and_b32_e32 v129, 0xffff0000, v232
	v_lshlrev_b32_e32 v232, 16, v233
	v_pk_mul_f32 v[130:131], v[238:239], v[238:239]
	v_pk_fma_f32 v[138:139], v[194:195], v[194:195], v[2:3] op_sel_hi:[1,1,0]
	v_pk_fma_f32 v[140:141], v[234:235], v[234:235], v[228:229] op_sel_hi:[1,1,0]
	v_and_b32_e32 v233, 0xffff0000, v233
	v_mul_f32_e32 v132, v128, v128
	v_mul_f32_e32 v134, v232, v232
	v_mov_b32_e32 v136, v124
	v_pk_fma_f32 v[130:131], v[236:237], v[236:237], v[130:131]
	v_mov_b32_e32 v125, v139
	v_mov_b32_e32 v137, v141
	v_pk_fma_f32 v[132:133], v[128:129], v[128:129], v[132:133] op_sel_hi:[1,1,0]
	v_pk_fma_f32 v[134:135], v[232:233], v[232:233], v[134:135] op_sel_hi:[1,1,0]
	v_pk_add_f32 v[130:131], v[130:131], v[130:131] op_sel_hi:[0,1]
	v_pk_add_f32 v[138:139], v[138:139], v[140:141]
	v_pk_mul_f32 v[136:137], v[124:125], v[136:137]
	v_mul_f32_e32 v132, v126, v126
	v_mul_f32_e32 v134, v127, v127
	v_mul_f32_e32 v130, v142, v142
	v_mov_b32_e32 v137, v139
	v_pk_add_f32 v[132:133], v[132:133], v[134:135]
	v_pk_add_f32 v[130:131], v[136:137], v[130:131]
	v_lshlrev_b32_e32 v134, 16, v231
	v_pk_add_f32 v[130:131], v[130:131], v[132:133]
	v_lshlrev_b32_e32 v132, 16, v230
	v_add_f32_e32 v2, v130, v131
	v_and_b32_e32 v135, 0xffff0000, v231
	v_lshlrev_b32_e32 v116, 16, v192
	v_add_f32_dpp v2, v2, v2 quad_perm:[1,0,3,2] row_mask:0xf bank_mask:0xf bound_ctrl:1
	v_and_b32_e32 v117, 0xffff0000, v192
	v_lshlrev_b32_e32 v192, 16, v193
	v_add_f32_dpp v2, v2, v2 quad_perm:[2,3,0,1] row_mask:0xf bank_mask:0xf bound_ctrl:1
	v_and_b32_e32 v193, 0xffff0000, v193
	s_nop 0
	v_add_f32_dpp v2, v2, v2 row_half_mirror row_mask:0xf bank_mask:0xf bound_ctrl:1
	s_nop 1
	v_add_f32_dpp v2, v2, v2 row_mirror row_mask:0xf bank_mask:0xf bound_ctrl:1
	s_nop 0
	v_readlane_b32 s1, v2, 16
	v_readlane_b32 s4, v2, 48
	v_readlane_b32 s2, v2, 0
	v_readlane_b32 s3, v2, 32
	v_mov_b32_e32 v130, s1
	v_mov_b32_e32 v131, s4
	v_pk_add_f32 v[130:131], s[2:3], v[130:131]
	s_mov_b64 s[4:5], -1
	v_add_f32_e32 v2, v130, v131
	v_fmamk_f32 v2, v2, 0x3a800000, v214
	v_lshlrev_b32_e32 v130, 16, v229
	v_and_b32_e32 v131, 0xffff0000, v229
	v_and_b32_e32 v133, 0xffff0000, v230
	v_rsq_f32_e32 v2, v2
	s_nop 0
	v_mul_f32_e32 v2, 0.5, v2
	v_pk_mul_f32 v[228:229], v[2:3], v[194:195] op_sel_hi:[0,1]
	v_pk_mul_f32 v[194:195], v[2:3], v[234:235] op_sel_hi:[0,1]
	v_pk_fma_f32 v[194:195], v[10:11], v[194:195], v[192:193]
	v_pk_fma_f32 v[192:193], v[8:9], v[228:229], v[116:117]
	v_mov_b32_e32 v228, v236
	v_mov_b32_e32 v229, v238
	v_mov_b32_e32 v238, v237
	v_pk_mul_f32 v[236:237], v[2:3], v[128:129] op_sel_hi:[0,1]
	v_pk_mul_f32 v[232:233], v[2:3], v[232:233] op_sel_hi:[0,1]
	v_mov_b32_e32 v125, v142
	v_pk_mul_f32 v[228:229], v[2:3], v[228:229] op_sel_hi:[0,1]
	v_pk_mul_f32 v[230:231], v[2:3], v[238:239] op_sel_hi:[0,1]
	v_pk_fma_f32 v[234:235], v[18:19], v[232:233], v[130:131]
	v_pk_fma_f32 v[232:233], v[16:17], v[236:237], v[122:123]
	v_pk_mul_f32 v[236:237], v[124:125], v[2:3] op_sel_hi:[1,0]
	v_pk_mul_f32 v[238:239], v[126:127], v[2:3] op_sel_hi:[1,0]
	v_cndmask_b32_e64 v2, 0, 1, s[6:7]
	v_pk_fma_f32 v[230:231], v[6:7], v[230:231], v[120:121]
	v_pk_fma_f32 v[228:229], v[4:5], v[228:229], v[118:119]
	v_pk_fma_f32 v[238:239], v[14:15], v[238:239], v[134:135]
	v_pk_fma_f32 v[236:237], v[12:13], v[236:237], v[132:133]
	v_cmp_ne_u32_e64 s[2:3], 1, v2
	s_andn2_b64 vcc, exec, s[6:7]
	v_lshl_add_u64 v[116:117], s[18:19], 0, v[100:101]
	s_cbranch_vccnz .LBB0_736_B
	v_pk_mul_f32 v[118:119], v[194:195], v[194:195]
	v_pk_mul_f32 v[120:121], v[192:193], v[192:193]
	v_mul_f32_e32 v2, v232, v232
	v_pk_mov_b32 v[122:123], v[120:121], v[118:119] op_sel:[1,0]
	v_mov_b32_e32 v121, v119
	v_pk_add_f32 v[118:119], v[122:123], v[120:121]
	v_pk_mul_f32 v[120:121], v[230:231], v[230:231]
	v_pk_mul_f32 v[122:123], v[228:229], v[228:229]
	v_pk_add_f32 v[118:119], v[118:119], v[118:119] op_sel_hi:[0,1]
	v_pk_mov_b32 v[124:125], v[122:123], v[120:121] op_sel:[1,0]
	v_mov_b32_e32 v123, v121
	v_pk_add_f32 v[120:121], v[124:125], v[122:123]
	v_pk_fma_f32 v[122:123], v[232:233], v[232:233], v[2:3] op_sel_hi:[1,1,0]
	v_mul_f32_e32 v2, v234, v234
	v_pk_add_f32 v[120:121], v[120:121], v[120:121] op_sel_hi:[0,1]
	v_pk_fma_f32 v[124:125], v[234:235], v[234:235], v[2:3] op_sel_hi:[1,1,0]
	v_mul_f32_e32 v122, v236, v236
	v_mul_f32_e32 v124, v237, v237
	v_mul_f32_e32 v118, v238, v238
	v_mul_f32_e32 v120, v239, v239
	v_pk_add_f32 v[122:123], v[122:123], v[124:125]
	v_pk_add_f32 v[118:119], v[118:119], v[120:121]
	v_cvt_pk_bf16_f32 v124, v236, v237
	v_cvt_pk_bf16_f32 v125, v238, v239
	s_nop 0
	v_pk_add_f32 v[118:119], v[122:123], v[118:119]
	v_cvt_pk_bf16_f32 v123, v234, v235
	s_nop 0
	v_add_f32_e32 v2, v118, v119
	s_nop 1
	v_add_f32_dpp v2, v2, v2 quad_perm:[1,0,3,2] row_mask:0xf bank_mask:0xf bound_ctrl:1
	s_nop 1
	v_add_f32_dpp v2, v2, v2 quad_perm:[2,3,0,1] row_mask:0xf bank_mask:0xf bound_ctrl:1
; __device__ __forceinline__ unsigned pk2(float lo, float hi) { unsigned r; asm("v_cvt_pk_bf16_f32 %0, %1, %2" : "=v"(r) : "v"(lo), "v"(hi)); return r; }
; __device__ __forceinline__ void thin_pass(const Ctx& C, const bf16* hin, bf16* hout, bf16* u, float* out, const bf16* y, const float* gpost, float cmul, const float* gpre, bool last) {
;     ...
;             if (last) { f32x4* op = (f32x4*)(out + (size_t)m * D); op[2 * lane] = h[0]; op[2 * lane + 1] = h[1]; op[128 + 2 * lane] = h[2]; op[128 + 2 * lane + 1] = h[3]; }
;             else {
;                 float s2 = 0.f;
; #pragma unroll
;                 for (int i = 0; i < 4; ++i) s2 += (h[i][0] * h[i][0] + h[i][1] * h[i][1]) + (h[i][2] * h[i][2] + h[i][3] * h[i][3]);
;                 const float rh = 1.0f / sqrtf(wave_sum(s2) * (1.0f / D) + RMS_EPS);
;                 v4u o0, o1; o0.x = pk2(h[0][0], h[0][1]); o0.y = pk2(h[0][2], h[0][3]); o0.z = pk2(h[1][0], h[1][1]); o0.w = pk2(h[1][2], h[1][3]);
;                 o1.x = pk2(h[2][0], h[2][1]); o1.y = pk2(h[2][2], h[2][3]); o1.z = pk2(h[3][0], h[3][1]); o1.w = pk2(h[3][2], h[3][3]);
;                 v4u* hp = (v4u*)(hout + (size_t)m * D); hp[lane] = o0; hp[64 + lane] = o1;
; #pragma unroll
;                 for (int i = 0; i < 4; ++i) h[i] = h[i] * rh * q4[i];
;                 o0.x = pk2(h[0][0], h[0][1]); o0.y = pk2(h[0][2], h[0][3]); o0.z = pk2(h[1][0], h[1][1]); o0.w = pk2(h[1][2], h[1][3]);
;                 o1.x = pk2(h[2][0], h[2][1]); o1.y = pk2(h[2][2], h[2][3]); o1.z = pk2(h[3][0], h[3][1]); o1.w = pk2(h[3][2], h[3][3]);
;                 v4u* up = (v4u*)(u + (size_t)m * D); up[lane] = o0; up[64 + lane] = o1;
	s_nop 1
	v_add_f32_dpp v2, v2, v2 row_half_mirror row_mask:0xf bank_mask:0xf bound_ctrl:1
	s_nop 1
	v_add_f32_dpp v2, v2, v2 row_mirror row_mask:0xf bank_mask:0xf bound_ctrl:1
	s_nop 0
	v_readlane_b32 s1, v2, 16
	v_readlane_b32 s9, v2, 48
	v_readlane_b32 s4, v2, 0
	v_readlane_b32 s5, v2, 32
	v_mov_b32_e32 v118, s1
	v_mov_b32_e32 v119, s9
	v_pk_add_f32 v[118:119], s[4:5], v[118:119]
	s_brev_b32 s1, 64
	v_add_f32_e32 v2, v118, v119
	v_fmamk_f32 v2, v2, 0x3a800000, v214
	s_mov_b64 s[4:5], 0
	v_add_co_u32_e32 v126, vcc, s1, v116
	v_rsq_f32_e32 v2, v2
	s_nop 0
	v_cvt_pk_bf16_f32 v118, v192, v193
	v_cvt_pk_bf16_f32 v119, v194, v195
	v_cvt_pk_bf16_f32 v120, v228, v229
	v_cvt_pk_bf16_f32 v121, v230, v231
	v_cvt_pk_bf16_f32 v122, v232, v233
	s_nop 0
	v_addc_co_u32_e32 v127, vcc, 0, v117, vcc
	global_store_dwordx4 v[126:127], v[118:121], off sc1
	global_store_dwordx4 v[126:127], v[122:125], off offset:1024 sc1
	v_pk_mul_f32 v[126:127], v[232:233], v[2:3] op_sel_hi:[1,0]
	v_pk_mul_f32 v[118:119], v[192:193], v[2:3] op_sel_hi:[1,0]
	v_pk_mul_f32 v[120:121], v[194:195], v[2:3] op_sel_hi:[1,0]
	v_pk_mul_f32 v[122:123], v[228:229], v[2:3] op_sel_hi:[1,0]
	v_pk_mul_f32 v[120:121], v[26:27], v[120:121]
	v_pk_mul_f32 v[118:119], v[24:25], v[118:119]
	v_pk_mul_f32 v[122:123], v[20:21], v[122:123]
	v_pk_mul_f32 v[126:127], v[32:33], v[126:127]
	v_pk_mul_f32 v[124:125], v[230:231], v[2:3] op_sel_hi:[1,0]
	v_cvt_pk_bf16_f32 v118, v118, v119
	v_cvt_pk_bf16_f32 v119, v120, v121
	v_cvt_pk_bf16_f32 v120, v122, v123
	v_cvt_pk_bf16_f32 v122, v126, v127
	v_add_co_u32_e32 v126, vcc, 0xb000000, v240
	v_pk_mul_f32 v[124:125], v[22:23], v[124:125]
	v_pk_mul_f32 v[128:129], v[234:235], v[2:3] op_sel_hi:[1,0]
	v_pk_mul_f32 v[130:131], v[236:237], v[2:3] op_sel_hi:[1,0]
	v_pk_mul_f32 v[132:133], v[238:239], v[2:3] op_sel_hi:[1,0]
	v_cvt_pk_bf16_f32 v121, v124, v125
	v_addc_co_u32_e32 v127, vcc, 0, v241, vcc
	v_pk_mul_f32 v[128:129], v[34:35], v[128:129]
	v_pk_mul_f32 v[132:133], v[30:31], v[132:133]
	v_pk_mul_f32 v[130:131], v[28:29], v[130:131]
	v_cvt_pk_bf16_f32 v123, v128, v129
	v_cvt_pk_bf16_f32 v125, v132, v133
	s_nop 0
	v_cvt_pk_bf16_f32 v124, v130, v131
	flat_store_dwordx4 v[126:127], v[118:121] sc1
	flat_store_dwordx4 v[126:127], v[122:125] offset:1024 sc1
.LBB0_736_B:
	s_andn2_b64 vcc, exec, s[4:5]
	s_cbranch_vccnz .LBB0_738_B
	v_add_co_u32_e32 v118, vcc, 0xffffe000, v112
	s_nop 1
	v_addc_co_u32_e32 v119, vcc, -1, v113, vcc
	global_store_dwordx4 v[118:119], v[192:195], off offset:-2064 sc1
	global_store_dwordx4 v[118:119], v[228:231], off offset:-2048 sc1
	global_store_dwordx4 v[118:119], v[232:235], off offset:-16 sc1
	global_store_dwordx4 v[118:119], v[236:239], off sc1
.LBB0_738_B:
	s_nop 0
	v_lshlrev_b32_e32 v232, 16, v184
	v_and_b32_e32 v233, 0xffff0000, v184
	v_mul_f32_e32 v2, v232, v232
	v_lshlrev_b32_e32 v184, 16, v185
	v_pk_fma_f32 v[234:235], v[232:233], v[232:233], v[2:3] op_sel_hi:[1,1,0]
	v_and_b32_e32 v185, 0xffff0000, v185
	v_mul_f32_e32 v2, v184, v184
	v_lshlrev_b32_e32 v239, 16, v187
	v_lshlrev_b32_e32 v238, 16, v186
	v_and_b32_e32 v187, 0xffff0000, v187
	v_and_b32_e32 v186, 0xffff0000, v186
	v_lshlrev_b32_e32 v120, 16, v180
	v_lshlrev_b32_e32 v192, 16, v182
	v_pk_fma_f32 v[236:237], v[184:185], v[184:185], v[2:3] op_sel_hi:[1,1,0]
	v_pk_mul_f32 v[118:119], v[186:187], v[186:187]
	v_and_b32_e32 v121, 0xffff0000, v180
	v_mul_f32_e32 v2, v120, v120
	v_lshlrev_b32_e32 v124, 16, v181
	v_pk_fma_f32 v[118:119], v[238:239], v[238:239], v[118:119]
	v_pk_fma_f32 v[122:123], v[120:121], v[120:121], v[2:3] op_sel_hi:[1,1,0]
	v_and_b32_e32 v125, 0xffff0000, v181
	v_mul_f32_e32 v2, v124, v124
	v_mov_b32_e32 v193, v235
	v_mov_b32_e32 v126, v192
	v_mov_b32_e32 v127, v237
	v_and_b32_e32 v128, 0xffff0000, v182
	v_lshlrev_b32_e32 v194, 16, v183
	v_and_b32_e32 v195, 0xffff0000, v183
	v_pk_add_f32 v[118:119], v[118:119], v[118:119] op_sel_hi:[0,1]
	v_pk_fma_f32 v[180:181], v[124:125], v[124:125], v[2:3] op_sel_hi:[1,1,0]
	v_pk_mul_f32 v[126:127], v[192:193], v[126:127]
	v_pk_add_f32 v[234:235], v[234:235], v[236:237]
	v_mul_f32_e32 v118, v128, v128
	v_mul_f32_e32 v122, v194, v194
	v_mul_f32_e32 v180, v195, v195
	v_mov_b32_e32 v127, v235
	v_pk_add_f32 v[234:235], v[126:127], v[118:119]
	v_pk_add_f32 v[180:181], v[122:123], v[180:181]
	v_lshlrev_b32_e32 v230, 16, v176
	v_pk_add_f32 v[180:181], v[234:235], v[180:181]
	v_and_b32_e32 v231, 0xffff0000, v176
	v_add_f32_e32 v2, v180, v181
	v_lshlrev_b32_e32 v234, 16, v177
	v_and_b32_e32 v235, 0xffff0000, v177
	v_add_f32_dpp v2, v2, v2 quad_perm:[1,0,3,2] row_mask:0xf bank_mask:0xf bound_ctrl:1
	v_lshlrev_b32_e32 v236, 16, v178
	v_and_b32_e32 v237, 0xffff0000, v178
	v_add_f32_dpp v2, v2, v2 quad_perm:[2,3,0,1] row_mask:0xf bank_mask:0xf bound_ctrl:1
	v_lshlrev_b32_e32 v118, 16, v179
	v_and_b32_e32 v119, 0xffff0000, v179
	v_add_f32_dpp v2, v2, v2 row_half_mirror row_mask:0xf bank_mask:0xf bound_ctrl:1
	v_lshlrev_b32_e32 v182, 16, v188
	v_and_b32_e32 v183, 0xffff0000, v188
	v_add_f32_dpp v2, v2, v2 row_mirror row_mask:0xf bank_mask:0xf bound_ctrl:1
	v_lshlrev_b32_e32 v188, 16, v189
	v_readlane_b32 s1, v2, 16
	v_readlane_b32 s9, v2, 48
	v_readlane_b32 s4, v2, 0
	v_readlane_b32 s5, v2, 32
	v_mov_b32_e32 v180, s1
	v_mov_b32_e32 v181, s9
	v_pk_add_f32 v[180:181], s[4:5], v[180:181]
	v_and_b32_e32 v189, 0xffff0000, v189
	v_add_f32_e32 v2, v180, v181
	v_fmamk_f32 v2, v2, 0x3a800000, v214
	v_mov_b32_e32 v181, v186
	v_mov_b32_e32 v186, v239
	v_lshlrev_b32_e32 v228, 16, v190
	v_and_b32_e32 v229, 0xffff0000, v190
	v_lshlrev_b32_e32 v190, 16, v191
	v_and_b32_e32 v191, 0xffff0000, v191
	v_mov_b32_e32 v193, v128
	s_mov_b64 s[4:5], -1
	v_rsq_f32_e32 v2, v2
	s_nop 0
	v_mul_f32_e32 v2, 0.5, v2
	v_pk_mul_f32 v[176:177], v[2:3], v[232:233] op_sel_hi:[0,1]
	v_pk_mul_f32 v[178:179], v[2:3], v[184:185] op_sel_hi:[0,1]
	v_pk_fma_f32 v[176:177], v[8:9], v[176:177], v[182:183]
	v_mov_b32_e32 v180, v238
	v_pk_mul_f32 v[182:183], v[2:3], v[186:187] op_sel_hi:[0,1]
	v_pk_fma_f32 v[178:179], v[10:11], v[178:179], v[188:189]
	v_pk_mul_f32 v[180:181], v[2:3], v[180:181] op_sel_hi:[0,1]
	v_pk_fma_f32 v[182:183], v[6:7], v[182:183], v[190:191]
	v_pk_mul_f32 v[184:185], v[2:3], v[120:121] op_sel_hi:[0,1]
	v_pk_mul_f32 v[186:187], v[2:3], v[124:125] op_sel_hi:[0,1]
	v_pk_mul_f32 v[188:189], v[192:193], v[2:3] op_sel_hi:[1,0]
	v_pk_mul_f32 v[190:191], v[194:195], v[2:3] op_sel_hi:[1,0]
	v_pk_fma_f32 v[180:181], v[4:5], v[180:181], v[228:229]
	v_pk_fma_f32 v[186:187], v[18:19], v[186:187], v[234:235]
	v_pk_fma_f32 v[184:185], v[16:17], v[184:185], v[230:231]
	v_pk_fma_f32 v[190:191], v[14:15], v[190:191], v[118:119]
	v_pk_fma_f32 v[188:189], v[12:13], v[188:189], v[236:237]
	s_and_b64 vcc, exec, s[2:3]
	s_cbranch_vccnz .LBB0_740_B
; __device__ __forceinline__ unsigned pk2(float lo, float hi) { unsigned r; asm("v_cvt_pk_bf16_f32 %0, %1, %2" : "=v"(r) : "v"(lo), "v"(hi)); return r; }
; __device__ __forceinline__ void thin_pass(const Ctx& C, const bf16* hin, bf16* hout, bf16* u, float* out, const bf16* y, const float* gpost, float cmul, const float* gpre, bool last) {
;     ...
;                 float s2 = 0.f;
; #pragma unroll
;                 for (int i = 0; i < 4; ++i) s2 += (h[i][0] * h[i][0] + h[i][1] * h[i][1]) + (h[i][2] * h[i][2] + h[i][3] * h[i][3]);
;                 const float rh = 1.0f / sqrtf(wave_sum(s2) * (1.0f / D) + RMS_EPS);
;                 v4u o0, o1; o0.x = pk2(h[0][0], h[0][1]); o0.y = pk2(h[0][2], h[0][3]); o0.z = pk2(h[1][0], h[1][1]); o0.w = pk2(h[1][2], h[1][3]);
;                 o1.x = pk2(h[2][0], h[2][1]); o1.y = pk2(h[2][2], h[2][3]); o1.z = pk2(h[3][0], h[3][1]); o1.w = pk2(h[3][2], h[3][3]);
;                 v4u* hp = (v4u*)(hout + (size_t)m * D); hp[lane] = o0; hp[64 + lane] = o1;
; #pragma unroll
;                 for (int i = 0; i < 4; ++i) h[i] = h[i] * rh * q4[i];
;                 o0.x = pk2(h[0][0], h[0][1]); o0.y = pk2(h[0][2], h[0][3]); o0.z = pk2(h[1][0], h[1][1]); o0.w = pk2(h[1][2], h[1][3]);
;                 o1.x = pk2(h[2][0], h[2][1]); o1.y = pk2(h[2][2], h[2][3]); o1.z = pk2(h[3][0], h[3][1]); o1.w = pk2(h[3][2], h[3][3]);
;                 v4u* up = (v4u*)(u + (size_t)m * D); up[lane] = o0; up[64 + lane] = o1;
	v_pk_mul_f32 v[192:193], v[178:179], v[178:179]
	v_pk_mul_f32 v[194:195], v[176:177], v[176:177]
	v_mul_f32_e32 v2, v184, v184
	v_pk_mov_b32 v[228:229], v[194:195], v[192:193] op_sel:[1,0]
	v_mov_b32_e32 v195, v193
	v_pk_add_f32 v[192:193], v[228:229], v[194:195]
	v_pk_mul_f32 v[194:195], v[182:183], v[182:183]
	v_pk_mul_f32 v[228:229], v[180:181], v[180:181]
	v_pk_add_f32 v[192:193], v[192:193], v[192:193] op_sel_hi:[0,1]
	v_pk_mov_b32 v[230:231], v[228:229], v[194:195] op_sel:[1,0]
	v_mov_b32_e32 v229, v195
	v_pk_add_f32 v[194:195], v[230:231], v[228:229]
	v_pk_fma_f32 v[228:229], v[184:185], v[184:185], v[2:3] op_sel_hi:[1,1,0]
	v_mul_f32_e32 v2, v186, v186
	v_pk_add_f32 v[194:195], v[194:195], v[194:195] op_sel_hi:[0,1]
	v_pk_fma_f32 v[230:231], v[186:187], v[186:187], v[2:3] op_sel_hi:[1,1,0]
	v_mul_f32_e32 v228, v188, v188
	v_mul_f32_e32 v230, v189, v189
	v_mul_f32_e32 v192, v190, v190
	v_mul_f32_e32 v194, v191, v191
	v_pk_add_f32 v[228:229], v[228:229], v[230:231]
	v_pk_add_f32 v[192:193], v[192:193], v[194:195]
	v_cvt_pk_bf16_f32 v230, v188, v189
	v_cvt_pk_bf16_f32 v231, v190, v191
	s_nop 0
	v_pk_add_f32 v[192:193], v[228:229], v[192:193]
	v_cvt_pk_bf16_f32 v229, v186, v187
	s_nop 0
	v_add_f32_e32 v2, v192, v193
	s_nop 1
	v_add_f32_dpp v2, v2, v2 quad_perm:[1,0,3,2] row_mask:0xf bank_mask:0xf bound_ctrl:1
	s_nop 1
	v_add_f32_dpp v2, v2, v2 quad_perm:[2,3,0,1] row_mask:0xf bank_mask:0xf bound_ctrl:1
	s_nop 1
	v_add_f32_dpp v2, v2, v2 row_half_mirror row_mask:0xf bank_mask:0xf bound_ctrl:1
	s_nop 1
	v_add_f32_dpp v2, v2, v2 row_mirror row_mask:0xf bank_mask:0xf bound_ctrl:1
	s_nop 0
	v_readlane_b32 s1, v2, 16
	v_readlane_b32 s9, v2, 48
	v_readlane_b32 s4, v2, 0
	v_readlane_b32 s5, v2, 32
	v_mov_b32_e32 v192, s1
	v_mov_b32_e32 v193, s9
	v_pk_add_f32 v[192:193], s[4:5], v[192:193]
	s_brev_b32 s1, 64
	v_add_f32_e32 v2, v192, v193
	v_fmamk_f32 v2, v2, 0x3a800000, v214
	s_mov_b64 s[4:5], 0
	v_add_co_u32_e32 v232, vcc, s1, v116
	v_rsq_f32_e32 v2, v2
	s_nop 0
	v_cvt_pk_bf16_f32 v192, v176, v177
	v_cvt_pk_bf16_f32 v193, v178, v179
	v_cvt_pk_bf16_f32 v194, v180, v181
	v_cvt_pk_bf16_f32 v195, v182, v183
	v_cvt_pk_bf16_f32 v228, v184, v185
	s_nop 0
	v_addc_co_u32_e32 v233, vcc, 0, v117, vcc
	global_store_dwordx4 v[232:233], v[192:195], off offset:2048 sc1
	global_store_dwordx4 v[232:233], v[228:231], off offset:3072 sc1
	v_pk_mul_f32 v[232:233], v[184:185], v[2:3] op_sel_hi:[1,0]
	v_pk_mul_f32 v[192:193], v[176:177], v[2:3] op_sel_hi:[1,0]
	v_pk_mul_f32 v[194:195], v[178:179], v[2:3] op_sel_hi:[1,0]
	v_pk_mul_f32 v[228:229], v[180:181], v[2:3] op_sel_hi:[1,0]
	v_pk_mul_f32 v[194:195], v[26:27], v[194:195]
	v_pk_mul_f32 v[192:193], v[24:25], v[192:193]
	v_pk_mul_f32 v[228:229], v[20:21], v[228:229]
	v_pk_mul_f32 v[232:233], v[32:33], v[232:233]
	v_pk_mul_f32 v[230:231], v[182:183], v[2:3] op_sel_hi:[1,0]
	v_cvt_pk_bf16_f32 v192, v192, v193
	v_cvt_pk_bf16_f32 v193, v194, v195
	v_cvt_pk_bf16_f32 v194, v228, v229
	v_cvt_pk_bf16_f32 v228, v232, v233
	v_add_co_u32_e32 v232, vcc, 0xb000000, v240
	v_pk_mul_f32 v[230:231], v[22:23], v[230:231]
	v_pk_mul_f32 v[234:235], v[186:187], v[2:3] op_sel_hi:[1,0]
	v_pk_mul_f32 v[236:237], v[188:189], v[2:3] op_sel_hi:[1,0]
	v_pk_mul_f32 v[238:239], v[190:191], v[2:3] op_sel_hi:[1,0]
	v_cvt_pk_bf16_f32 v195, v230, v231
	v_addc_co_u32_e32 v233, vcc, 0, v241, vcc
	v_pk_mul_f32 v[234:235], v[34:35], v[234:235]
	v_pk_mul_f32 v[238:239], v[30:31], v[238:239]
	v_pk_mul_f32 v[236:237], v[28:29], v[236:237]
	v_cvt_pk_bf16_f32 v229, v234, v235
	v_cvt_pk_bf16_f32 v231, v238, v239
	s_nop 0
	v_cvt_pk_bf16_f32 v230, v236, v237
	flat_store_dwordx4 v[232:233], v[192:195] offset:2048 sc1
	flat_store_dwordx4 v[232:233], v[228:231] offset:3072 sc1
.LBB0_740_B:
	s_andn2_b64 vcc, exec, s[4:5]
	s_cbranch_vccnz .LBB0_742_B
	v_add_co_u32_e32 v192, vcc, 0xfffff000, v112
	s_nop 1
	v_addc_co_u32_e32 v193, vcc, -1, v113, vcc
	global_store_dwordx4 v[192:193], v[176:179], off offset:-2064 sc1
	global_store_dwordx4 v[192:193], v[180:183], off offset:-2048 sc1
	global_store_dwordx4 v[192:193], v[184:187], off offset:-16 sc1
	global_store_dwordx4 v[112:113], v[188:191], off offset:-4096 sc1
.LBB0_742_B:
	s_nop 0
	v_lshlrev_b32_e32 v184, 16, v168
	v_and_b32_e32 v185, 0xffff0000, v168
	v_mul_f32_e32 v2, v184, v184
	v_lshlrev_b32_e32 v168, 16, v169
	v_pk_fma_f32 v[186:187], v[184:185], v[184:185], v[2:3] op_sel_hi:[1,1,0]
	v_and_b32_e32 v169, 0xffff0000, v169
	v_mul_f32_e32 v2, v168, v168
	v_lshlrev_b32_e32 v191, 16, v171
	v_lshlrev_b32_e32 v190, 16, v170
	v_and_b32_e32 v171, 0xffff0000, v171
	v_and_b32_e32 v170, 0xffff0000, v170
	v_lshlrev_b32_e32 v194, 16, v164
	v_lshlrev_b32_e32 v176, 16, v166
	v_pk_fma_f32 v[188:189], v[168:169], v[168:169], v[2:3] op_sel_hi:[1,1,0]
	v_pk_mul_f32 v[192:193], v[170:171], v[170:171]
	v_and_b32_e32 v195, 0xffff0000, v164
	v_mul_f32_e32 v2, v194, v194
	v_lshlrev_b32_e32 v230, 16, v165
	v_pk_fma_f32 v[192:193], v[190:191], v[190:191], v[192:193]
	v_pk_fma_f32 v[228:229], v[194:195], v[194:195], v[2:3] op_sel_hi:[1,1,0]
	v_and_b32_e32 v231, 0xffff0000, v165
	v_mul_f32_e32 v2, v230, v230
	v_mov_b32_e32 v177, v187
	v_mov_b32_e32 v232, v176
	v_mov_b32_e32 v233, v189
	v_and_b32_e32 v234, 0xffff0000, v166
	v_lshlrev_b32_e32 v178, 16, v167
	v_and_b32_e32 v179, 0xffff0000, v167
	v_pk_add_f32 v[192:193], v[192:193], v[192:193] op_sel_hi:[0,1]
	v_pk_fma_f32 v[164:165], v[230:231], v[230:231], v[2:3] op_sel_hi:[1,1,0]
	v_pk_mul_f32 v[232:233], v[176:177], v[232:233]
	v_pk_add_f32 v[186:187], v[186:187], v[188:189]
	v_mul_f32_e32 v192, v234, v234
	v_mul_f32_e32 v228, v178, v178
	v_mul_f32_e32 v164, v179, v179
; __device__ __forceinline__ unsigned pk2(float lo, float hi) { unsigned r; asm("v_cvt_pk_bf16_f32 %0, %1, %2" : "=v"(r) : "v"(lo), "v"(hi)); return r; }
; __device__ __forceinline__ void thin_pass(const Ctx& C, const bf16* hin, bf16* hout, bf16* u, float* out, const bf16* y, const float* gpost, float cmul, const float* gpre, bool last) {
;     ...
;             float ss = 0.f;
; #pragma unroll
;             for (int i = 0; i < 4; ++i) ss += (yv[i][0] * yv[i][0] + yv[i][1] * yv[i][1]) + (yv[i][2] * yv[i][2] + yv[i][3] * yv[i][3]);
;             const float ry = cmul / sqrtf(wave_sum(ss) * (1.0f / D) + RMS_EPS);
; #pragma unroll
;             for (int i = 0; i < 4; ++i) h[i] = h[i] + yv[i] * ry * g4[i];
;             if (last) { f32x4* op = (f32x4*)(out + (size_t)m * D); op[2 * lane] = h[0]; op[2 * lane + 1] = h[1]; op[128 + 2 * lane] = h[2]; op[128 + 2 * lane + 1] = h[3]; }
;             else {
;                 float s2 = 0.f;
; #pragma unroll
;                 for (int i = 0; i < 4; ++i) s2 += (h[i][0] * h[i][0] + h[i][1] * h[i][1]) + (h[i][2] * h[i][2] + h[i][3] * h[i][3]);
;                 const float rh = 1.0f / sqrtf(wave_sum(s2) * (1.0f / D) + RMS_EPS);
;                 v4u o0, o1; o0.x = pk2(h[0][0], h[0][1]); o0.y = pk2(h[0][2], h[0][3]); o0.z = pk2(h[1][0], h[1][1]); o0.w = pk2(h[1][2], h[1][3]);
;                 o1.x = pk2(h[2][0], h[2][1]); o1.y = pk2(h[2][2], h[2][3]); o1.z = pk2(h[3][0], h[3][1]); o1.w = pk2(h[3][2], h[3][3]);
;                 v4u* hp = (v4u*)(hout + (size_t)m * D); hp[lane] = o0; hp[64 + lane] = o1;
; #pragma unroll
;                 for (int i = 0; i < 4; ++i) h[i] = h[i] * rh * q4[i];
;                 o0.x = pk2(h[0][0], h[0][1]); o0.y = pk2(h[0][2], h[0][3]); o0.z = pk2(h[1][0], h[1][1]); o0.w = pk2(h[1][2], h[1][3]);
;                 o1.x = pk2(h[2][0], h[2][1]); o1.y = pk2(h[2][2], h[2][3]); o1.z = pk2(h[3][0], h[3][1]); o1.w = pk2(h[3][2], h[3][3]);
;                 v4u* up = (v4u*)(u + (size_t)m * D); up[lane] = o0; up[64 + lane] = o1;
	v_mov_b32_e32 v233, v187
	v_pk_add_f32 v[186:187], v[232:233], v[192:193]
	v_pk_add_f32 v[164:165], v[228:229], v[164:165]
	v_lshlrev_b32_e32 v182, 16, v160
	v_pk_add_f32 v[164:165], v[186:187], v[164:165]
	v_and_b32_e32 v183, 0xffff0000, v160
	v_add_f32_e32 v2, v164, v165
	v_lshlrev_b32_e32 v186, 16, v161
	v_and_b32_e32 v187, 0xffff0000, v161
	v_add_f32_dpp v2, v2, v2 quad_perm:[1,0,3,2] row_mask:0xf bank_mask:0xf bound_ctrl:1
	v_lshlrev_b32_e32 v188, 16, v162
	v_and_b32_e32 v189, 0xffff0000, v162
	v_add_f32_dpp v2, v2, v2 quad_perm:[2,3,0,1] row_mask:0xf bank_mask:0xf bound_ctrl:1
	v_lshlrev_b32_e32 v192, 16, v163
	v_and_b32_e32 v193, 0xffff0000, v163
	v_add_f32_dpp v2, v2, v2 row_half_mirror row_mask:0xf bank_mask:0xf bound_ctrl:1
	v_lshlrev_b32_e32 v166, 16, v172
	v_and_b32_e32 v167, 0xffff0000, v172
	v_add_f32_dpp v2, v2, v2 row_mirror row_mask:0xf bank_mask:0xf bound_ctrl:1
	v_lshlrev_b32_e32 v172, 16, v173
	v_readlane_b32 s1, v2, 16
	v_readlane_b32 s9, v2, 48
	v_readlane_b32 s4, v2, 0
	v_readlane_b32 s5, v2, 32
	v_mov_b32_e32 v164, s1
	v_mov_b32_e32 v165, s9
	v_pk_add_f32 v[164:165], s[4:5], v[164:165]
	v_and_b32_e32 v173, 0xffff0000, v173
	v_add_f32_e32 v2, v164, v165
	v_fmamk_f32 v2, v2, 0x3a800000, v214
	v_mov_b32_e32 v165, v170
	v_mov_b32_e32 v170, v191
	v_lshlrev_b32_e32 v180, 16, v174
	v_and_b32_e32 v181, 0xffff0000, v174
	v_lshlrev_b32_e32 v174, 16, v175
	v_and_b32_e32 v175, 0xffff0000, v175
	v_mov_b32_e32 v177, v234
	s_mov_b64 s[4:5], -1
	v_rsq_f32_e32 v2, v2
	s_nop 0
	v_mul_f32_e32 v2, 0.5, v2
	v_pk_mul_f32 v[160:161], v[2:3], v[184:185] op_sel_hi:[0,1]
	v_pk_mul_f32 v[162:163], v[2:3], v[168:169] op_sel_hi:[0,1]
	v_pk_fma_f32 v[160:161], v[8:9], v[160:161], v[166:167]
	v_mov_b32_e32 v164, v190
	v_pk_mul_f32 v[166:167], v[2:3], v[170:171] op_sel_hi:[0,1]
	v_pk_fma_f32 v[162:163], v[10:11], v[162:163], v[172:173]
	v_pk_mul_f32 v[164:165], v[2:3], v[164:165] op_sel_hi:[0,1]
	v_pk_fma_f32 v[166:167], v[6:7], v[166:167], v[174:175]
	v_pk_mul_f32 v[168:169], v[2:3], v[194:195] op_sel_hi:[0,1]
	v_pk_mul_f32 v[170:171], v[2:3], v[230:231] op_sel_hi:[0,1]
	v_pk_mul_f32 v[172:173], v[176:177], v[2:3] op_sel_hi:[1,0]
	v_pk_mul_f32 v[174:175], v[178:179], v[2:3] op_sel_hi:[1,0]
	v_pk_fma_f32 v[164:165], v[4:5], v[164:165], v[180:181]
	v_pk_fma_f32 v[170:171], v[18:19], v[170:171], v[186:187]
	v_pk_fma_f32 v[168:169], v[16:17], v[168:169], v[182:183]
	v_pk_fma_f32 v[174:175], v[14:15], v[174:175], v[192:193]
	v_pk_fma_f32 v[172:173], v[12:13], v[172:173], v[188:189]
	s_and_b64 vcc, exec, s[2:3]
	s_cbranch_vccnz .LBB0_744_B
	v_pk_mul_f32 v[176:177], v[162:163], v[162:163]
	v_pk_mul_f32 v[178:179], v[160:161], v[160:161]
	v_mul_f32_e32 v2, v168, v168
	v_pk_mov_b32 v[180:181], v[178:179], v[176:177] op_sel:[1,0]
	v_mov_b32_e32 v179, v177
	v_pk_add_f32 v[176:177], v[180:181], v[178:179]
	v_pk_mul_f32 v[178:179], v[166:167], v[166:167]
	v_pk_mul_f32 v[180:181], v[164:165], v[164:165]
	v_pk_add_f32 v[176:177], v[176:177], v[176:177] op_sel_hi:[0,1]
	v_pk_mov_b32 v[182:183], v[180:181], v[178:179] op_sel:[1,0]
	v_mov_b32_e32 v181, v179
	v_pk_add_f32 v[178:179], v[182:183], v[180:181]
	v_pk_fma_f32 v[180:181], v[168:169], v[168:169], v[2:3] op_sel_hi:[1,1,0]
	v_mul_f32_e32 v2, v170, v170
	v_pk_add_f32 v[178:179], v[178:179], v[178:179] op_sel_hi:[0,1]
	v_pk_fma_f32 v[182:183], v[170:171], v[170:171], v[2:3] op_sel_hi:[1,1,0]
	v_mul_f32_e32 v180, v172, v172
	v_mul_f32_e32 v182, v173, v173
	v_mul_f32_e32 v176, v174, v174
	v_mul_f32_e32 v178, v175, v175
	v_pk_add_f32 v[180:181], v[180:181], v[182:183]
	v_pk_add_f32 v[176:177], v[176:177], v[178:179]
	v_cvt_pk_bf16_f32 v182, v172, v173
	v_cvt_pk_bf16_f32 v183, v174, v175
	s_nop 0
	v_pk_add_f32 v[176:177], v[180:181], v[176:177]
	v_cvt_pk_bf16_f32 v181, v170, v171
	s_nop 0
	v_add_f32_e32 v2, v176, v177
	s_nop 1
	v_add_f32_dpp v2, v2, v2 quad_perm:[1,0,3,2] row_mask:0xf bank_mask:0xf bound_ctrl:1
	s_nop 1
	v_add_f32_dpp v2, v2, v2 quad_perm:[2,3,0,1] row_mask:0xf bank_mask:0xf bound_ctrl:1
	s_nop 1
	v_add_f32_dpp v2, v2, v2 row_half_mirror row_mask:0xf bank_mask:0xf bound_ctrl:1
	s_nop 1
	v_add_f32_dpp v2, v2, v2 row_mirror row_mask:0xf bank_mask:0xf bound_ctrl:1
	s_nop 0
	v_readlane_b32 s1, v2, 16
	v_readlane_b32 s9, v2, 48
	v_readlane_b32 s4, v2, 0
	v_readlane_b32 s5, v2, 32
	v_mov_b32_e32 v176, s1
	v_mov_b32_e32 v177, s9
	v_pk_add_f32 v[176:177], s[4:5], v[176:177]
	s_nop 0
	v_add_f32_e32 v2, v176, v177
	v_fmamk_f32 v2, v2, 0x3a800000, v214
	s_mov_b64 s[4:5], 0
	v_add_co_u32_e32 v184, vcc, s93, v116
	v_rsq_f32_e32 v2, v2
	s_nop 0
	v_cvt_pk_bf16_f32 v176, v160, v161
	v_cvt_pk_bf16_f32 v177, v162, v163
	v_cvt_pk_bf16_f32 v178, v164, v165
	v_cvt_pk_bf16_f32 v179, v166, v167
	v_cvt_pk_bf16_f32 v180, v168, v169
	s_nop 0
	v_addc_co_u32_e32 v185, vcc, 0, v117, vcc
	global_store_dwordx4 v[184:185], v[176:179], off sc1
	global_store_dwordx4 v[184:185], v[180:183], off offset:1024 sc1
	v_pk_mul_f32 v[184:185], v[168:169], v[2:3] op_sel_hi:[1,0]
	v_pk_mul_f32 v[176:177], v[160:161], v[2:3] op_sel_hi:[1,0]
	v_pk_mul_f32 v[178:179], v[162:163], v[2:3] op_sel_hi:[1,0]
	v_pk_mul_f32 v[180:181], v[164:165], v[2:3] op_sel_hi:[1,0]
	v_pk_mul_f32 v[178:179], v[26:27], v[178:179]
	v_pk_mul_f32 v[176:177], v[24:25], v[176:177]
	v_pk_mul_f32 v[180:181], v[20:21], v[180:181]
	v_pk_mul_f32 v[184:185], v[32:33], v[184:185]
	v_pk_mul_f32 v[182:183], v[166:167], v[2:3] op_sel_hi:[1,0]
	v_cvt_pk_bf16_f32 v176, v176, v177
	v_cvt_pk_bf16_f32 v177, v178, v179
	v_cvt_pk_bf16_f32 v178, v180, v181
	v_cvt_pk_bf16_f32 v180, v184, v185
	v_add_co_u32_e32 v184, vcc, 0xb001000, v240
	v_pk_mul_f32 v[182:183], v[22:23], v[182:183]
	v_pk_mul_f32 v[186:187], v[170:171], v[2:3] op_sel_hi:[1,0]
	v_pk_mul_f32 v[188:189], v[172:173], v[2:3] op_sel_hi:[1,0]
	v_pk_mul_f32 v[190:191], v[174:175], v[2:3] op_sel_hi:[1,0]
	v_cvt_pk_bf16_f32 v179, v182, v183
	v_addc_co_u32_e32 v185, vcc, 0, v241, vcc
	v_pk_mul_f32 v[186:187], v[34:35], v[186:187]
	v_pk_mul_f32 v[190:191], v[30:31], v[190:191]
	v_pk_mul_f32 v[188:189], v[28:29], v[188:189]
	v_cvt_pk_bf16_f32 v181, v186, v187
	v_cvt_pk_bf16_f32 v183, v190, v191
	s_nop 0
	v_cvt_pk_bf16_f32 v182, v188, v189
	flat_store_dwordx4 v[184:185], v[176:179] sc1
	flat_store_dwordx4 v[184:185], v[180:183] offset:1024 sc1
; __device__ __forceinline__ void thin_pass(const Ctx& C, const bf16* hin, bf16* hout, bf16* u, float* out, const bf16* y, const float* gpost, float cmul, const float* gpre, bool last) {
;     ...
;         for (int b = 0; b < RB; ++b) {
;             const int m = m0 + b; const v4u y0 = yr[b][0], y1 = yr[b][1], h0 = hr[b][0], h1 = hr[b][1];
;             f32x4 yv[4], h[4];
;             yv[0] = (f32x4){bf_lo(y0.x), bf_hi(y0.x), bf_lo(y0.y), bf_hi(y0.y)}; yv[1] = (f32x4){bf_lo(y0.z), bf_hi(y0.z), bf_lo(y0.w), bf_hi(y0.w)};
;             yv[2] = (f32x4){bf_lo(y1.x), bf_hi(y1.x), bf_lo(y1.y), bf_hi(y1.y)}; yv[3] = (f32x4){bf_lo(y1.z), bf_hi(y1.z), bf_lo(y1.w), bf_hi(y1.w)};
;             h[0] = (f32x4){bf_lo(h0.x), bf_hi(h0.x), bf_lo(h0.y), bf_hi(h0.y)}; h[1] = (f32x4){bf_lo(h0.z), bf_hi(h0.z), bf_lo(h0.w), bf_hi(h0.w)};
;             h[2] = (f32x4){bf_lo(h1.x), bf_hi(h1.x), bf_lo(h1.y), bf_hi(h1.y)}; h[3] = (f32x4){bf_lo(h1.z), bf_hi(h1.z), bf_lo(h1.w), bf_hi(h1.w)};
;             float ss = 0.f;
; #pragma unroll
;             for (int i = 0; i < 4; ++i) ss += (yv[i][0] * yv[i][0] + yv[i][1] * yv[i][1]) + (yv[i][2] * yv[i][2] + yv[i][3] * yv[i][3]);
;             const float ry = cmul / sqrtf(wave_sum(ss) * (1.0f / D) + RMS_EPS);
; #pragma unroll
;             for (int i = 0; i < 4; ++i) h[i] = h[i] + yv[i] * ry * g4[i];
;             if (last) { f32x4* op = (f32x4*)(out + (size_t)m * D); op[2 * lane] = h[0]; op[2 * lane + 1] = h[1]; op[128 + 2 * lane] = h[2]; op[128 + 2 * lane + 1] = h[3]; }
;             else {
;                 float s2 = 0.f;
; #pragma unroll
;                 for (int i = 0; i < 4; ++i) s2 += (h[i][0] * h[i][0] + h[i][1] * h[i][1]) + (h[i][2] * h[i][2] + h[i][3] * h[i][3]);
;                 const float rh = 1.0f / sqrtf(wave_sum(s2) * (1.0f / D) + RMS_EPS);
;                 v4u o0, o1; o0.x = pk2(h[0][0], h[0][1]); o0.y = pk2(h[0][2], h[0][3]); o0.z = pk2(h[1][0], h[1][1]); o0.w = pk2(h[1][2], h[1][3]);
;                 o1.x = pk2(h[2][0], h[2][1]); o1.y = pk2(h[2][2], h[2][3]); o1.z = pk2(h[3][0], h[3][1]); o1.w = pk2(h[3][2], h[3][3]);
;                 v4u* hp = (v4u*)(hout + (size_t)m * D); hp[lane] = o0; hp[64 + lane] = o1;
; #pragma unroll
;                 for (int i = 0; i < 4; ++i) h[i] = h[i] * rh * q4[i];
.LBB0_744_B:
	s_andn2_b64 vcc, exec, s[4:5]
	s_cbranch_vccnz .LBB0_746_B
	global_store_dwordx4 v[112:113], v[160:163], off offset:-2064 sc1
	global_store_dwordx4 v[112:113], v[164:167], off offset:-2048 sc1
	global_store_dwordx4 v[112:113], v[168:171], off offset:-16 sc1
	global_store_dwordx4 v[112:113], v[172:175], off sc1
.LBB0_746_B:
	s_nop 0
	v_lshlrev_b32_e32 v168, 16, v152
	v_and_b32_e32 v169, 0xffff0000, v152
	v_mul_f32_e32 v2, v168, v168
	v_lshlrev_b32_e32 v152, 16, v153
	v_pk_fma_f32 v[170:171], v[168:169], v[168:169], v[2:3] op_sel_hi:[1,1,0]
	v_and_b32_e32 v153, 0xffff0000, v153
	v_mul_f32_e32 v2, v152, v152
	v_lshlrev_b32_e32 v175, 16, v155
	v_lshlrev_b32_e32 v174, 16, v154
	v_and_b32_e32 v155, 0xffff0000, v155
	v_and_b32_e32 v154, 0xffff0000, v154
	v_lshlrev_b32_e32 v178, 16, v148
	v_lshlrev_b32_e32 v160, 16, v150
	v_pk_fma_f32 v[172:173], v[152:153], v[152:153], v[2:3] op_sel_hi:[1,1,0]
	v_pk_mul_f32 v[176:177], v[154:155], v[154:155]
	v_and_b32_e32 v179, 0xffff0000, v148
	v_mul_f32_e32 v2, v178, v178
	v_lshlrev_b32_e32 v182, 16, v149
	v_pk_fma_f32 v[176:177], v[174:175], v[174:175], v[176:177]
	v_pk_fma_f32 v[180:181], v[178:179], v[178:179], v[2:3] op_sel_hi:[1,1,0]
	v_and_b32_e32 v183, 0xffff0000, v149
	v_mul_f32_e32 v2, v182, v182
	v_mov_b32_e32 v161, v171
	v_mov_b32_e32 v184, v160
	v_mov_b32_e32 v185, v173
	v_and_b32_e32 v186, 0xffff0000, v150
	v_lshlrev_b32_e32 v162, 16, v151
	v_and_b32_e32 v163, 0xffff0000, v151
	v_pk_add_f32 v[176:177], v[176:177], v[176:177] op_sel_hi:[0,1]
	v_pk_fma_f32 v[148:149], v[182:183], v[182:183], v[2:3] op_sel_hi:[1,1,0]
	v_pk_mul_f32 v[184:185], v[160:161], v[184:185]
	v_pk_add_f32 v[170:171], v[170:171], v[172:173]
	v_mul_f32_e32 v176, v186, v186
	v_mul_f32_e32 v180, v162, v162
	v_mul_f32_e32 v148, v163, v163
	v_mov_b32_e32 v185, v171
	v_pk_add_f32 v[170:171], v[184:185], v[176:177]
	v_pk_add_f32 v[148:149], v[180:181], v[148:149]
	v_lshlrev_b32_e32 v166, 16, v144
	v_pk_add_f32 v[148:149], v[170:171], v[148:149]
	v_and_b32_e32 v167, 0xffff0000, v144
	v_add_f32_e32 v2, v148, v149
	v_lshlrev_b32_e32 v170, 16, v145
	v_and_b32_e32 v171, 0xffff0000, v145
	v_add_f32_dpp v2, v2, v2 quad_perm:[1,0,3,2] row_mask:0xf bank_mask:0xf bound_ctrl:1
	v_lshlrev_b32_e32 v172, 16, v146
	v_and_b32_e32 v173, 0xffff0000, v146
	v_add_f32_dpp v2, v2, v2 quad_perm:[2,3,0,1] row_mask:0xf bank_mask:0xf bound_ctrl:1
	v_lshlrev_b32_e32 v176, 16, v147
	v_and_b32_e32 v177, 0xffff0000, v147
	v_add_f32_dpp v2, v2, v2 row_half_mirror row_mask:0xf bank_mask:0xf bound_ctrl:1
	v_lshlrev_b32_e32 v150, 16, v156
	v_and_b32_e32 v151, 0xffff0000, v156
	v_add_f32_dpp v2, v2, v2 row_mirror row_mask:0xf bank_mask:0xf bound_ctrl:1
	v_lshlrev_b32_e32 v156, 16, v157
	v_readlane_b32 s1, v2, 16
	v_readlane_b32 s9, v2, 48
	v_readlane_b32 s4, v2, 0
	v_readlane_b32 s5, v2, 32
	v_mov_b32_e32 v148, s1
	v_mov_b32_e32 v149, s9
	v_pk_add_f32 v[148:149], s[4:5], v[148:149]
	v_and_b32_e32 v157, 0xffff0000, v157
	v_add_f32_e32 v2, v148, v149
	v_fmamk_f32 v2, v2, 0x3a800000, v214
	v_mov_b32_e32 v149, v154
	v_mov_b32_e32 v154, v175
	v_lshlrev_b32_e32 v164, 16, v158
	v_and_b32_e32 v165, 0xffff0000, v158
	v_lshlrev_b32_e32 v158, 16, v159
	v_and_b32_e32 v159, 0xffff0000, v159
	v_mov_b32_e32 v161, v186
	v_rsq_f32_e32 v2, v2
	s_nop 0
	v_mul_f32_e32 v2, 0.5, v2
	v_pk_mul_f32 v[144:145], v[2:3], v[168:169] op_sel_hi:[0,1]
	v_pk_mul_f32 v[146:147], v[2:3], v[152:153] op_sel_hi:[0,1]
	v_pk_fma_f32 v[144:145], v[8:9], v[144:145], v[150:151]
	v_mov_b32_e32 v148, v174
	v_pk_mul_f32 v[150:151], v[2:3], v[154:155] op_sel_hi:[0,1]
	v_pk_fma_f32 v[146:147], v[10:11], v[146:147], v[156:157]
	v_pk_mul_f32 v[148:149], v[2:3], v[148:149] op_sel_hi:[0,1]
	v_pk_fma_f32 v[150:151], v[6:7], v[150:151], v[158:159]
	v_pk_mul_f32 v[152:153], v[2:3], v[178:179] op_sel_hi:[0,1]
	v_pk_mul_f32 v[154:155], v[2:3], v[182:183] op_sel_hi:[0,1]
	v_pk_mul_f32 v[156:157], v[160:161], v[2:3] op_sel_hi:[1,0]
	v_pk_mul_f32 v[158:159], v[162:163], v[2:3] op_sel_hi:[1,0]
	v_pk_fma_f32 v[148:149], v[4:5], v[148:149], v[164:165]
	v_pk_fma_f32 v[154:155], v[18:19], v[154:155], v[170:171]
	v_pk_fma_f32 v[152:153], v[16:17], v[152:153], v[166:167]
	v_pk_fma_f32 v[158:159], v[14:15], v[158:159], v[176:177]
	v_pk_fma_f32 v[156:157], v[12:13], v[156:157], v[172:173]
	s_and_b64 vcc, exec, s[2:3]
	s_mov_b64 s[2:3], -1
	s_cbranch_vccnz .LBB0_748_B
; __device__ __forceinline__ unsigned pk2(float lo, float hi) { unsigned r; asm("v_cvt_pk_bf16_f32 %0, %1, %2" : "=v"(r) : "v"(lo), "v"(hi)); return r; }
; __device__ __forceinline__ void thin_pass(const Ctx& C, const bf16* hin, bf16* hout, bf16* u, float* out, const bf16* y, const float* gpost, float cmul, const float* gpre, bool last) {
;     ...
;                 float s2 = 0.f;
; #pragma unroll
;                 for (int i = 0; i < 4; ++i) s2 += (h[i][0] * h[i][0] + h[i][1] * h[i][1]) + (h[i][2] * h[i][2] + h[i][3] * h[i][3]);
;                 const float rh = 1.0f / sqrtf(wave_sum(s2) * (1.0f / D) + RMS_EPS);
;                 v4u o0, o1; o0.x = pk2(h[0][0], h[0][1]); o0.y = pk2(h[0][2], h[0][3]); o0.z = pk2(h[1][0], h[1][1]); o0.w = pk2(h[1][2], h[1][3]);
;                 o1.x = pk2(h[2][0], h[2][1]); o1.y = pk2(h[2][2], h[2][3]); o1.z = pk2(h[3][0], h[3][1]); o1.w = pk2(h[3][2], h[3][3]);
;                 v4u* hp = (v4u*)(hout + (size_t)m * D); hp[lane] = o0; hp[64 + lane] = o1;
; #pragma unroll
;                 for (int i = 0; i < 4; ++i) h[i] = h[i] * rh * q4[i];
;                 o0.x = pk2(h[0][0], h[0][1]); o0.y = pk2(h[0][2], h[0][3]); o0.z = pk2(h[1][0], h[1][1]); o0.w = pk2(h[1][2], h[1][3]);
;                 o1.x = pk2(h[2][0], h[2][1]); o1.y = pk2(h[2][2], h[2][3]); o1.z = pk2(h[3][0], h[3][1]); o1.w = pk2(h[3][2], h[3][3]);
;                 v4u* up = (v4u*)(u + (size_t)m * D); up[lane] = o0; up[64 + lane] = o1;
	v_pk_mul_f32 v[160:161], v[146:147], v[146:147]
	v_pk_mul_f32 v[162:163], v[144:145], v[144:145]
	v_mul_f32_e32 v2, v152, v152
	v_pk_mov_b32 v[164:165], v[162:163], v[160:161] op_sel:[1,0]
	v_mov_b32_e32 v163, v161
	v_pk_add_f32 v[160:161], v[164:165], v[162:163]
	v_pk_mul_f32 v[162:163], v[150:151], v[150:151]
	v_pk_mul_f32 v[164:165], v[148:149], v[148:149]
	v_pk_add_f32 v[160:161], v[160:161], v[160:161] op_sel_hi:[0,1]
	v_pk_mov_b32 v[166:167], v[164:165], v[162:163] op_sel:[1,0]
	v_mov_b32_e32 v165, v163
	v_pk_add_f32 v[162:163], v[166:167], v[164:165]
	v_pk_fma_f32 v[164:165], v[152:153], v[152:153], v[2:3] op_sel_hi:[1,1,0]
	v_mul_f32_e32 v2, v154, v154
	v_pk_add_f32 v[162:163], v[162:163], v[162:163] op_sel_hi:[0,1]
	v_pk_fma_f32 v[166:167], v[154:155], v[154:155], v[2:3] op_sel_hi:[1,1,0]
	v_mul_f32_e32 v164, v156, v156
	v_mul_f32_e32 v166, v157, v157
	v_mul_f32_e32 v160, v158, v158
	v_mul_f32_e32 v162, v159, v159
	v_pk_add_f32 v[164:165], v[164:165], v[166:167]
	v_pk_add_f32 v[160:161], v[160:161], v[162:163]
	v_cvt_pk_bf16_f32 v166, v156, v157
	v_cvt_pk_bf16_f32 v167, v158, v159
	s_nop 0
	v_pk_add_f32 v[160:161], v[164:165], v[160:161]
	v_cvt_pk_bf16_f32 v165, v154, v155
	s_nop 0
	v_add_f32_e32 v2, v160, v161
	s_nop 1
	v_add_f32_dpp v2, v2, v2 quad_perm:[1,0,3,2] row_mask:0xf bank_mask:0xf bound_ctrl:1
	s_nop 1
	v_add_f32_dpp v2, v2, v2 quad_perm:[2,3,0,1] row_mask:0xf bank_mask:0xf bound_ctrl:1
	s_nop 1
	v_add_f32_dpp v2, v2, v2 row_half_mirror row_mask:0xf bank_mask:0xf bound_ctrl:1
	s_nop 1
	v_add_f32_dpp v2, v2, v2 row_mirror row_mask:0xf bank_mask:0xf bound_ctrl:1
	s_nop 0
	v_readlane_b32 s1, v2, 16
	v_readlane_b32 s4, v2, 48
	v_readlane_b32 s2, v2, 0
	v_readlane_b32 s3, v2, 32
	v_mov_b32_e32 v160, s1
	v_mov_b32_e32 v161, s4
	v_pk_add_f32 v[160:161], s[2:3], v[160:161]
	s_nop 0
	v_add_f32_e32 v2, v160, v161
	v_fmamk_f32 v2, v2, 0x3a800000, v214
	s_lshl_b64 s[2:3], s[42:43], 10
	s_lshl_b64 s[2:3], s[2:3], 1
	v_lshl_add_u64 v[168:169], v[106:107], 0, s[2:3]
	v_rsq_f32_e32 v2, v2
	s_nop 0
	v_cvt_pk_bf16_f32 v160, v144, v145
	v_cvt_pk_bf16_f32 v161, v146, v147
	v_cvt_pk_bf16_f32 v162, v148, v149
	v_cvt_pk_bf16_f32 v163, v150, v151
	v_cvt_pk_bf16_f32 v164, v152, v153
	global_store_dwordx4 v[168:169], v[160:163], off sc1
	global_store_dwordx4 v[168:169], v[164:167], off offset:1024 sc1
	v_pk_mul_f32 v[168:169], v[152:153], v[2:3] op_sel_hi:[1,0]
	v_pk_mul_f32 v[160:161], v[144:145], v[2:3] op_sel_hi:[1,0]
	v_pk_mul_f32 v[162:163], v[146:147], v[2:3] op_sel_hi:[1,0]
	v_pk_mul_f32 v[164:165], v[148:149], v[2:3] op_sel_hi:[1,0]
	v_pk_mul_f32 v[162:163], v[26:27], v[162:163]
	v_pk_mul_f32 v[160:161], v[24:25], v[160:161]
	v_pk_mul_f32 v[166:167], v[150:151], v[2:3] op_sel_hi:[1,0]
	v_pk_mul_f32 v[164:165], v[20:21], v[164:165]
	v_pk_mul_f32 v[168:169], v[32:33], v[168:169]
	v_pk_mul_f32 v[166:167], v[22:23], v[166:167]
	v_pk_mul_f32 v[170:171], v[154:155], v[2:3] op_sel_hi:[1,0]
	v_pk_mul_f32 v[172:173], v[156:157], v[2:3] op_sel_hi:[1,0]
	v_pk_mul_f32 v[174:175], v[158:159], v[2:3] op_sel_hi:[1,0]
	v_cvt_pk_bf16_f32 v160, v160, v161
	v_cvt_pk_bf16_f32 v161, v162, v163
	v_cvt_pk_bf16_f32 v162, v164, v165
	v_cvt_pk_bf16_f32 v163, v166, v167
	v_cvt_pk_bf16_f32 v164, v168, v169
	v_lshl_add_u64 v[168:169], v[108:109], 0, s[2:3]
	s_mov_b64 s[2:3], 0
	v_pk_mul_f32 v[170:171], v[34:35], v[170:171]
	v_pk_mul_f32 v[174:175], v[30:31], v[174:175]
	v_pk_mul_f32 v[172:173], v[28:29], v[172:173]
	v_cvt_pk_bf16_f32 v165, v170, v171
	v_cvt_pk_bf16_f32 v167, v174, v175
	s_nop 0
	v_cvt_pk_bf16_f32 v166, v172, v173
	flat_store_dwordx4 v[168:169], v[160:163] sc1
	flat_store_dwordx4 v[168:169], v[164:167] offset:1024 sc1
.LBB0_748_B:
	s_andn2_b64 vcc, exec, s[2:3]
	s_cbranch_vccnz .LBB0_733_B
	s_lshl_b64 s[2:3], s[42:43], 12
	v_lshl_add_u64 v[160:161], v[110:111], 0, s[2:3]
	global_store_dwordx4 v[160:161], v[144:147], off sc1
	global_store_dwordx4 v[160:161], v[148:151], off offset:16 sc1
	global_store_dwordx4 v[160:161], v[152:155], off offset:2048 sc1
	global_store_dwordx4 v[160:161], v[156:159], off offset:2064 sc1
	s_branch .LBB0_733_B
